# v14
# speedup vs baseline: 1.0057x; 1.0003x over previous
_Z9nerf_mainPKfS0_S0_PKiS2_PKcS0_Pf:
	s_load_dwordx8 s[8:15], s[0:1], 0x20
	s_load_dwordx8 s[24:31], s[0:1], 0x0
	v_readfirstlane_b32 s3, v0
	v_and_b32_e32 v120, 63, v0
	v_lshlrev_b32_e32 v121, 4, v120
	s_mov_b32 s39, 0x20000
	s_waitcnt lgkmcnt(0)
	s_load_dword s50, s[30:31], 0x0
	s_load_dword s51, s[8:9], 0x0
	s_load_dwordx8 s[52:59], s[28:29], 0x0
	s_load_dwordx4 s[60:63], s[28:29], 0x20
	s_lshr_b32 s64, s3, 7
	s_lshl_b32 s65, s2, 2
	s_add_i32 s64, s64, s65
	s_ashr_i32 s65, s64, 31
	s_lshl_b64 s[64:65], s[64:65], 2
	s_add_u32 s66, s24, s64
	s_addc_u32 s67, s25, s65
	s_add_u32 s64, s26, s64
	s_addc_u32 s65, s27, s65
	s_load_dword s68, s[66:67], 0x0
	s_load_dword s69, s[64:65], 0x0
	v_lshlrev_b32_e32 v188, 2, v0
	v_add_u32_e32 v189, 0x1000, v188
	global_load_dword v184, v188, s[12:13]
	global_load_dword v185, v188, s[12:13] offset:2048
	global_load_dword v186, v189, s[12:13]
	global_load_dword v187, v189, s[12:13] offset:2048
	s_and_b32 s37, s11, 0xffff
	s_lshl_b32 s11, s3, 4
	s_mov_b32 s38, 0xf0000
	s_and_b32 s42, s11, 0xfffffc00
	s_mov_b32 s4, s10
	s_mov_b32 s5, s37
	s_mov_b32 s6, s38
	s_mov_b32 s7, s39
	v_or_b32_e32 v125, s42, v121
	s_add_i32 m0, s42, 0x1a000
	s_movk_i32 s11, 0x2000
	buffer_load_dwordx4 v125, s[4:7], 0 offen lds
	s_add_i32 m0, s42, 0x1c000
	s_nop 0
	buffer_load_dwordx4 v125, s[4:7], s11 offen lds
	s_add_i32 m0, s42, 0x1e000
	s_movk_i32 s11, 0x4000
	buffer_load_dwordx4 v125, s[4:7], s11 offen lds
	s_add_i32 m0, s42, 0x20000
	s_movk_i32 s11, 0x6000
	buffer_load_dwordx4 v125, s[4:7], s11 offen lds
	s_add_i32 m0, s42, 0x22000
	s_mov_b32 s11, 0xe8000
	buffer_load_dwordx4 v125, s[4:7], s11 offen lds
	s_add_i32 m0, s42, 0xa000
	s_mov_b32 s11, 0x8000
	buffer_load_dwordx4 v125, s[4:7], s11 offen lds
	s_add_i32 m0, s42, 0xc000
	s_mov_b32 s11, 0xa000
	buffer_load_dwordx4 v125, s[4:7], s11 offen lds
	s_add_i32 m0, s42, 0xe000
	s_mov_b32 s11, 0xc000
	buffer_load_dwordx4 v125, s[4:7], s11 offen lds
	s_add_i32 m0, s42, 0x10000
	s_mov_b32 s11, 0xe000
	buffer_load_dwordx4 v125, s[4:7], s11 offen lds
	s_mov_b32 s36, s10
	s_waitcnt lgkmcnt(0)
	s_mov_b32 s0, s50
	s_lshl_b32 s1, s2, 2
	s_mov_b32 s2, s51
	s_lshr_b32 s31, s3, 7
	s_bfe_u32 s30, s3, 0x10006
	s_waitcnt lgkmcnt(0)
	v_cvt_f32_i32_e32 v1, s0
	s_add_i32 s12, s31, s1
	s_add_i32 s1, s0, 0xf423f
	s_cmp_lt_u32 s1, 0x1e847f
	v_mov_b32_e32 v2, s0
	s_cselect_b64 vcc, -1, 0
	v_cndmask_b32_e32 v123, v2, v1, vcc
	v_cvt_f32_i32_e32 v1, s2
	s_add_i32 s0, s2, 0xf423f
	s_cmp_lt_u32 s0, 0x1e847f
	v_mov_b32_e32 v2, s2
	s_cselect_b64 vcc, -1, 0
	v_cndmask_b32_e32 v1, v2, v1, vcc
	v_sub_f32_e32 v122, v1, v123
	s_mov_b32 s2, 0x427c0000
	v_div_scale_f32 v1, s[0:1], s2, s2, v122
	v_rcp_f32_e32 v2, v1
	s_ashr_i32 s13, s12, 31
	s_lshl_b64 s[0:1], s[12:13], 2
	s_add_u32 s4, s24, s0
	v_fma_f32 v5, -v1, v2, 1.0
	s_addc_u32 s5, s25, s1
	v_fmac_f32_e32 v2, v5, v2
	v_div_scale_f32 v5, vcc, v122, s2, v122
	s_add_u32 s0, s26, s0
	v_mul_f32_e32 v6, v5, v2
	s_mov_b64 s[16:17], s[52:53]
	s_mov_b64 s[18:19], s[54:55]
	s_mov_b64 s[20:21], s[56:57]
	s_mov_b64 s[22:23], s[58:59]
	s_addc_u32 s1, s27, s1
	v_fma_f32 v7, -v1, v6, v5
	s_mov_b32 s4, s68
	v_fmac_f32_e32 v6, v7, v2
	s_mov_b32 s0, s69
	v_fma_f32 v1, -v1, v6, v5
	v_div_fmas_f32 v1, v1, v2, v6
	v_div_fixup_f32 v124, v1, s2, v122
	s_waitcnt lgkmcnt(0)
	v_mov_b32_e32 v1, s16
	s_mov_b64 s[24:25], s[60:61]
	s_mov_b64 s[26:27], s[62:63]
	v_mul_f32_e32 v1, s4, v1
	v_mov_b32_e32 v2, s0
	v_fma_f32 v1, s17, -v2, v1
	v_add_f32_e32 v127, s19, v1
	v_mov_b32_e32 v1, s20
	v_mul_f32_e32 v1, s4, v1
	v_fma_f32 v1, s21, -v2, v1
	v_add_f32_e32 v128, s23, v1
	s_waitcnt lgkmcnt(0)
	v_mov_b32_e32 v1, s24
	v_mul_f32_e32 v1, s4, v1
	v_and_b32_e32 v3, 15, v0
	v_fma_f32 v1, s25, -v2, v1
	v_and_b32_e32 v131, 48, v0
	v_lshl_or_b32 v0, s30, 6, v120
	v_add_f32_e32 v129, s27, v1
	v_add_u32_e32 v1, 1, v0
	v_cvt_f32_ubyte0_e32 v1, v1
	s_mov_b32 s4, 0x43010000
	s_and_b32 s19, s3, 0xffffff80
	v_div_scale_f32 v2, s[2:3], s4, s4, v1
	v_lshl_or_b32 v130, s30, 5, v3
	v_rcp_f32_e32 v3, v2
	v_lshrrev_b32_e32 v4, 4, v120
	v_cmp_eq_u32_e64 s[8:9], 2, v4
	v_cmp_eq_u32_e64 s[10:11], 1, v4
	v_fma_f32 v5, -v2, v3, 1.0
	v_fmac_f32_e32 v3, v5, v3
	v_div_scale_f32 v5, vcc, v1, s4, v1
	v_mul_f32_e32 v6, v5, v3
	v_fma_f32 v7, -v2, v6, v5
	v_fmac_f32_e32 v6, v7, v3
	v_fma_f32 v2, -v2, v6, v5
	v_div_fmas_f32 v2, v2, v3, v6
	v_div_fixup_f32 v134, v2, s4, v1
	v_add_u32_e32 v2, -1, v4
	v_cmp_gt_u32_e32 vcc, 2, v2
	v_mov_b32_e32 v2, 0x401550d3
	v_mov_b32_e32 v3, 0x436d0620
	v_cndmask_b32_e64 v5, v2, v3, s[8:9]
	v_mov_b32_e32 v6, 0x412e2e5e
	v_cmp_eq_u32_e64 s[0:1], 3, v4
	v_cndmask_b32_e64 v4, v5, v6, s[10:11]
	v_cmp_gt_u32_e64 s[2:3], 16, v120
	v_bfrev_b32_e32 v5, 34
	v_mov_b32_e32 v8, 0x41bc2043
	v_cndmask_b32_e64 v140, v4, 0.5, s[2:3]
	v_mov_b32_e32 v4, 0x40a14518
	v_cndmask_b32_e64 v7, v4, v5, s[8:9]
	v_cndmask_b32_e64 v7, v7, v8, s[10:11]
	v_mov_b32_e32 v9, 0x3f8a3f66
	v_cndmask_b32_e64 v141, v7, v9, s[2:3]
	v_cndmask_b32_e64 v7, v6, 0.5, s[8:9]
	v_cndmask_b32_e64 v6, v3, v6, s[8:9]
	v_mov_b32_e32 v10, 0x424b2ff5
	v_cndmask_b32_e64 v6, v6, 0.5, s[10:11]
	v_cndmask_b32_e64 v144, v6, v10, s[2:3]
	v_cndmask_b32_e64 v6, v5, v8, s[8:9]
	v_or_b32_e32 v0, s19, v0
	v_mov_b32_e32 v11, 0x42db7457
	v_cndmask_b32_e64 v6, v6, v9, s[10:11]
	v_lshlrev_b32_e32 v0, 2, v0
	v_cndmask_b32_e64 v7, v7, v10, s[10:11]
	v_cndmask_b32_e64 v145, v6, v11, s[2:3]
	v_cndmask_b32_e64 v6, 0, v10, s[8:9]
	v_add_u32_e32 v135, 0x15000, v0
	v_add_u32_e32 v136, 0x15800, v0
	v_cvt_f32_ubyte0_e32 v0, v130
	v_or_b32_e32 v138, 16, v130
	v_cndmask_b32_e64 v142, v7, v2, s[2:3]
	v_cndmask_b32_e64 v2, v6, v2, s[10:11]
	s_lshl_b32 s13, s31, 10
	s_lshl_b32 s44, s31, 8
	v_fma_f32 v137, v0, v124, v123
	v_cvt_f32_ubyte0_e32 v0, v138
	v_cndmask_b32_e64 v7, v8, v9, s[8:9]
	v_cndmask_b32_e64 v146, v2, v3, s[2:3]
	v_cndmask_b32_e64 v2, 0, v11, s[8:9]
	s_lshl_b32 s27, s19, 2
	s_add_i32 s13, s13, 0x12000
	s_add_i32 s44, s44, 0x16000
	v_fma_f32 v139, v0, v124, v123
	v_lshlrev_b32_e32 v0, 4, v130
	v_lshlrev_b32_e32 v1, 4, v138
	v_cndmask_b32_e64 v7, v7, v11, s[10:11]
	v_cndmask_b32_e64 v2, v2, v4, s[10:11]
	v_or_b32_e32 v126, 0x2000, v121
	s_add_i32 s23, s27, 0x15000
	s_add_i32 s28, s42, 0xa000
	s_add_i32 s29, s42, 0xc000
	s_add_i32 s33, s42, 0xe000
	s_add_i32 s34, s42, 0x10000
	s_add_i32 s35, s42, 0x2000
	s_add_i32 s40, s42, 0x8000
	s_add_i32 s41, s42, 0x6000
	s_addk_i32 s42, 0x4000
	s_sub_i32 s43, s19, 64
	v_lshl_or_b32 v132, v120, 4, s13
	v_lshl_or_b32 v133, v120, 2, s44
	s_mov_b32 s20, 1
	s_or_b64 s[4:5], s[2:3], vcc
	s_or_b64 s[6:7], s[2:3], s[10:11]
	v_cndmask_b32_e64 v143, v7, v4, s[2:3]
	s_mov_b32 s45, 0
	v_cndmask_b32_e64 v147, v2, v5, s[2:3]
	v_or_b32_e32 v148, 0x1a000, v121
	v_or_b32_e32 v149, 0x1a400, v121
	v_or_b32_e32 v150, 0x1a800, v121
	v_or_b32_e32 v151, 0x1ac00, v121
	v_or_b32_e32 v152, 0x1b000, v121
	v_or_b32_e32 v153, 0x1b400, v121
	v_or_b32_e32 v154, 0x1b800, v121
	v_or_b32_e32 v155, 0x1bc00, v121
	v_or_b32_e32 v156, 0x1c000, v121
	v_or_b32_e32 v157, 0x1c400, v121
	v_or_b32_e32 v158, 0x1c800, v121
	v_or_b32_e32 v159, 0x1cc00, v121
	v_or_b32_e32 v160, 0x1d000, v121
	v_or_b32_e32 v161, 0x1d400, v121
	v_or_b32_e32 v162, 0x1d800, v121
	v_or_b32_e32 v163, 0x1dc00, v121
	v_or_b32_e32 v164, 0x1e000, v121
	v_or_b32_e32 v165, 0x1e400, v121
	v_or_b32_e32 v166, 0x1e800, v121
	v_or_b32_e32 v167, 0x1ec00, v121
	v_or_b32_e32 v168, 0x1f000, v121
	v_or_b32_e32 v169, 0x1f400, v121
	v_or_b32_e32 v170, 0x1f800, v121
	v_or_b32_e32 v171, 0x1fc00, v121
	v_or_b32_e32 v172, 0x20000, v121
	v_or_b32_e32 v173, 0x20400, v121
	v_or_b32_e32 v174, 0x20800, v121
	v_or_b32_e32 v175, 0x20c00, v121
	v_or_b32_e32 v176, 0x21000, v121
	v_or_b32_e32 v177, 0x21400, v121
	v_or_b32_e32 v178, 0x21800, v121
	v_or_b32_e32 v179, 0x21c00, v121
	v_add_u32_e32 v180, s13, v0
	v_add_u32_e32 v181, s13, v1
	v_mov_b32_e32 v182, 0x13000
	s_waitcnt vmcnt(9)
	ds_write_b32 v188, v184
	ds_write_b32 v188, v185 offset:2048
	ds_write_b32 v188, v186 offset:4096
	ds_write_b32 v188, v187 offset:6144
	s_branch .LBB1_5

.Lnerf_enc_done:
	v_mov_b32_e32 v183, v131
	s_mov_b32 s50, 0x10000
	s_mov_b32 s52, 0
	v_or_b32_e32 v88, 0x1a000, v121
	s_waitcnt vmcnt(0) lgkmcnt(0)
	s_barrier
	ds_read_b128 v[224:227], v88 offset:0
	ds_read_b128 v[228:231], v88 offset:1024
	ds_read_b128 v[232:235], v88 offset:2048
	ds_read_b128 v[236:239], v88 offset:3072
	ds_read_b128 v[240:243], v88 offset:4096
	ds_read_b128 v[244:247], v88 offset:5120
	ds_read_b128 v[248:251], v88 offset:6144
	ds_read_b128 v[252:255], v88 offset:7168
	s_waitcnt lgkmcnt(7)
	v_mfma_f32_16x16x32_bf16 v[64:67], v[224:227], v[208:211], 0
	v_mfma_f32_16x16x32_bf16 v[56:59], v[224:227], v[212:215], 0
	ds_read_b128 v[224:227], v88 offset:8192
	s_waitcnt lgkmcnt(7)
	v_mfma_f32_16x16x32_bf16 v[68:71], v[228:231], v[208:211], 0
	v_mfma_f32_16x16x32_bf16 v[60:63], v[228:231], v[212:215], 0
	ds_read_b128 v[228:231], v88 offset:9216
	s_waitcnt lgkmcnt(7)
	v_mfma_f32_16x16x32_bf16 v[64:67], v[232:235], v[216:219], v[64:67]
	v_mfma_f32_16x16x32_bf16 v[56:59], v[232:235], v[220:223], v[56:59]
	ds_read_b128 v[232:235], v88 offset:10240
	s_waitcnt lgkmcnt(7)
	v_mfma_f32_16x16x32_bf16 v[68:71], v[236:239], v[216:219], v[68:71]
	v_mfma_f32_16x16x32_bf16 v[60:63], v[236:239], v[220:223], v[60:63]
	ds_read_b128 v[236:239], v88 offset:11264
	s_waitcnt lgkmcnt(7)
	v_mfma_f32_16x16x32_bf16 v[80:83], v[240:243], v[208:211], 0
	v_cvt_pk_bf16_f32 v0, v64, v65
	v_cvt_pk_bf16_f32 v1, v66, v67
	v_mfma_f32_16x16x32_bf16 v[84:87], v[240:243], v[212:215], 0
	v_cvt_pk_bf16_f32 v4, v56, v57
	v_cvt_pk_bf16_f32 v5, v58, v59
	ds_read_b128 v[240:243], v88 offset:12288
	s_waitcnt lgkmcnt(7)
	v_mfma_f32_16x16x32_bf16 v[76:79], v[244:247], v[208:211], 0
	v_cvt_pk_bf16_f32 v2, v68, v69
	v_cvt_pk_bf16_f32 v3, v70, v71
	v_mfma_f32_16x16x32_bf16 v[72:75], v[244:247], v[212:215], 0
	v_cvt_pk_bf16_f32 v6, v60, v61
	v_cvt_pk_bf16_f32 v7, v62, v63
	ds_read_b128 v[244:247], v88 offset:13312
	s_waitcnt lgkmcnt(7)
	v_mfma_f32_16x16x32_bf16 v[80:83], v[248:251], v[216:219], v[80:83]
	v_pk_max_i16 v0, v0, 0
	v_pk_max_i16 v1, v1, 0
	v_mfma_f32_16x16x32_bf16 v[84:87], v[248:251], v[220:223], v[84:87]
	v_pk_max_i16 v2, v2, 0
	v_pk_max_i16 v3, v3, 0
	ds_read_b128 v[248:251], v88 offset:14336
	s_waitcnt lgkmcnt(7)
	v_mfma_f32_16x16x32_bf16 v[76:79], v[252:255], v[216:219], v[76:79]
	v_pk_max_i16 v4, v4, 0
	v_pk_max_i16 v5, v5, 0
	v_mfma_f32_16x16x32_bf16 v[72:75], v[252:255], v[220:223], v[72:75]
	v_pk_max_i16 v6, v6, 0
	v_pk_max_i16 v7, v7, 0
	ds_read_b128 v[252:255], v88 offset:15360
	s_waitcnt lgkmcnt(7)
	v_mfma_f32_16x16x32_bf16 v[64:67], v[224:227], v[208:211], 0
	v_cvt_pk_bf16_f32 v12, v80, v81
	v_cvt_pk_bf16_f32 v13, v82, v83
	v_mfma_f32_16x16x32_bf16 v[56:59], v[224:227], v[212:215], 0
	v_cvt_pk_bf16_f32 v8, v84, v85
	v_cvt_pk_bf16_f32 v9, v86, v87
	ds_read_b128 v[224:227], v88 offset:16384
	s_waitcnt lgkmcnt(7)
	v_mfma_f32_16x16x32_bf16 v[68:71], v[228:231], v[208:211], 0
	v_cvt_pk_bf16_f32 v14, v76, v77
	v_cvt_pk_bf16_f32 v15, v78, v79
	v_mfma_f32_16x16x32_bf16 v[60:63], v[228:231], v[212:215], 0
	v_cvt_pk_bf16_f32 v10, v72, v73
	v_cvt_pk_bf16_f32 v11, v74, v75
	ds_read_b128 v[228:231], v88 offset:17408
	s_waitcnt lgkmcnt(7)
	v_mfma_f32_16x16x32_bf16 v[64:67], v[232:235], v[216:219], v[64:67]
	v_pk_max_i16 v12, v12, 0
	v_pk_max_i16 v13, v13, 0
	v_mfma_f32_16x16x32_bf16 v[56:59], v[232:235], v[220:223], v[56:59]
	v_pk_max_i16 v14, v14, 0
	v_pk_max_i16 v15, v15, 0
	ds_read_b128 v[232:235], v88 offset:18432
	s_waitcnt lgkmcnt(7)
	v_mfma_f32_16x16x32_bf16 v[68:71], v[236:239], v[216:219], v[68:71]
	v_pk_max_i16 v8, v8, 0
	v_pk_max_i16 v9, v9, 0
	v_mfma_f32_16x16x32_bf16 v[60:63], v[236:239], v[220:223], v[60:63]
	v_pk_max_i16 v10, v10, 0
	v_pk_max_i16 v11, v11, 0
	ds_read_b128 v[236:239], v88 offset:19456
	s_waitcnt lgkmcnt(7)
	v_mfma_f32_16x16x32_bf16 v[80:83], v[240:243], v[208:211], 0
	v_cvt_pk_bf16_f32 v16, v64, v65
	v_cvt_pk_bf16_f32 v17, v66, v67
	v_mfma_f32_16x16x32_bf16 v[84:87], v[240:243], v[212:215], 0
	v_cvt_pk_bf16_f32 v20, v56, v57
	v_cvt_pk_bf16_f32 v21, v58, v59
	ds_read_b128 v[240:243], v88 offset:20480
	s_waitcnt lgkmcnt(7)
	v_mfma_f32_16x16x32_bf16 v[76:79], v[244:247], v[208:211], 0
	v_cvt_pk_bf16_f32 v18, v68, v69
	v_cvt_pk_bf16_f32 v19, v70, v71
	v_mfma_f32_16x16x32_bf16 v[72:75], v[244:247], v[212:215], 0
	v_cvt_pk_bf16_f32 v22, v60, v61
	v_cvt_pk_bf16_f32 v23, v62, v63
	ds_read_b128 v[244:247], v88 offset:21504
	s_waitcnt lgkmcnt(7)
	v_mfma_f32_16x16x32_bf16 v[80:83], v[248:251], v[216:219], v[80:83]
	v_pk_max_i16 v16, v16, 0
	v_pk_max_i16 v17, v17, 0
	v_mfma_f32_16x16x32_bf16 v[84:87], v[248:251], v[220:223], v[84:87]
	v_pk_max_i16 v18, v18, 0
	v_pk_max_i16 v19, v19, 0
	ds_read_b128 v[248:251], v88 offset:22528
	s_waitcnt lgkmcnt(7)
	v_mfma_f32_16x16x32_bf16 v[76:79], v[252:255], v[216:219], v[76:79]
	v_pk_max_i16 v20, v20, 0
	v_pk_max_i16 v21, v21, 0
	v_mfma_f32_16x16x32_bf16 v[72:75], v[252:255], v[220:223], v[72:75]
	v_pk_max_i16 v22, v22, 0
	v_pk_max_i16 v23, v23, 0
	ds_read_b128 v[252:255], v88 offset:23552
	s_waitcnt lgkmcnt(7)
	v_mfma_f32_16x16x32_bf16 v[64:67], v[224:227], v[208:211], 0
	v_cvt_pk_bf16_f32 v24, v80, v81
	v_cvt_pk_bf16_f32 v25, v82, v83
	v_mfma_f32_16x16x32_bf16 v[56:59], v[224:227], v[212:215], 0
	v_cvt_pk_bf16_f32 v28, v84, v85
	v_cvt_pk_bf16_f32 v29, v86, v87
	ds_read_b128 v[224:227], v88 offset:24576
	s_waitcnt lgkmcnt(7)
	v_mfma_f32_16x16x32_bf16 v[68:71], v[228:231], v[208:211], 0
	v_cvt_pk_bf16_f32 v26, v76, v77
	v_cvt_pk_bf16_f32 v27, v78, v79
	v_mfma_f32_16x16x32_bf16 v[60:63], v[228:231], v[212:215], 0
	v_cvt_pk_bf16_f32 v30, v72, v73
	v_cvt_pk_bf16_f32 v31, v74, v75
	ds_read_b128 v[228:231], v88 offset:25600
	s_waitcnt lgkmcnt(7)
	v_mfma_f32_16x16x32_bf16 v[64:67], v[232:235], v[216:219], v[64:67]
	v_pk_max_i16 v24, v24, 0
	v_pk_max_i16 v25, v25, 0
	v_mfma_f32_16x16x32_bf16 v[56:59], v[232:235], v[220:223], v[56:59]
	v_pk_max_i16 v26, v26, 0
	v_pk_max_i16 v27, v27, 0
	ds_read_b128 v[232:235], v88 offset:26624
	s_waitcnt lgkmcnt(7)
	v_mfma_f32_16x16x32_bf16 v[68:71], v[236:239], v[216:219], v[68:71]
	v_pk_max_i16 v28, v28, 0
	v_pk_max_i16 v29, v29, 0
	v_mfma_f32_16x16x32_bf16 v[60:63], v[236:239], v[220:223], v[60:63]
	v_pk_max_i16 v30, v30, 0
	v_pk_max_i16 v31, v31, 0
	ds_read_b128 v[236:239], v88 offset:27648
	s_waitcnt lgkmcnt(7)
	v_mfma_f32_16x16x32_bf16 v[80:83], v[240:243], v[208:211], 0
	v_cvt_pk_bf16_f32 v32, v64, v65
	v_cvt_pk_bf16_f32 v33, v66, v67
	v_mfma_f32_16x16x32_bf16 v[84:87], v[240:243], v[212:215], 0
	v_cvt_pk_bf16_f32 v36, v56, v57
	v_cvt_pk_bf16_f32 v37, v58, v59
	ds_read_b128 v[240:243], v88 offset:28672
	s_waitcnt lgkmcnt(7)
	v_mfma_f32_16x16x32_bf16 v[76:79], v[244:247], v[208:211], 0
	v_cvt_pk_bf16_f32 v34, v68, v69
	v_cvt_pk_bf16_f32 v35, v70, v71
	v_mfma_f32_16x16x32_bf16 v[72:75], v[244:247], v[212:215], 0
	v_cvt_pk_bf16_f32 v38, v60, v61
	v_cvt_pk_bf16_f32 v39, v62, v63
	ds_read_b128 v[244:247], v88 offset:29696
	s_waitcnt lgkmcnt(7)
	v_mfma_f32_16x16x32_bf16 v[80:83], v[248:251], v[216:219], v[80:83]
	v_pk_max_i16 v32, v32, 0
	v_pk_max_i16 v33, v33, 0
	v_mfma_f32_16x16x32_bf16 v[84:87], v[248:251], v[220:223], v[84:87]
	v_pk_max_i16 v34, v34, 0
	v_pk_max_i16 v35, v35, 0
	ds_read_b128 v[248:251], v88 offset:30720
	s_waitcnt lgkmcnt(7)
	v_mfma_f32_16x16x32_bf16 v[76:79], v[252:255], v[216:219], v[76:79]
	v_pk_max_i16 v36, v36, 0
	v_pk_max_i16 v37, v37, 0
	v_mfma_f32_16x16x32_bf16 v[72:75], v[252:255], v[220:223], v[72:75]
	v_pk_max_i16 v38, v38, 0
	v_pk_max_i16 v39, v39, 0
	ds_read_b128 v[252:255], v88 offset:31744
	s_waitcnt lgkmcnt(7)
	v_mfma_f32_16x16x32_bf16 v[64:67], v[224:227], v[208:211], 0
	v_cvt_pk_bf16_f32 v40, v80, v81
	v_cvt_pk_bf16_f32 v41, v82, v83
	v_mfma_f32_16x16x32_bf16 v[56:59], v[224:227], v[212:215], 0
	v_cvt_pk_bf16_f32 v44, v84, v85
	v_cvt_pk_bf16_f32 v45, v86, v87
	s_waitcnt lgkmcnt(6)
	v_mfma_f32_16x16x32_bf16 v[68:71], v[228:231], v[208:211], 0
	v_cvt_pk_bf16_f32 v42, v76, v77
	v_cvt_pk_bf16_f32 v43, v78, v79
	v_mfma_f32_16x16x32_bf16 v[60:63], v[228:231], v[212:215], 0
	v_cvt_pk_bf16_f32 v46, v72, v73
	v_cvt_pk_bf16_f32 v47, v74, v75
	s_waitcnt lgkmcnt(5)
	v_mfma_f32_16x16x32_bf16 v[64:67], v[232:235], v[216:219], v[64:67]
	v_pk_max_i16 v40, v40, 0
	v_pk_max_i16 v41, v41, 0
	v_mfma_f32_16x16x32_bf16 v[56:59], v[232:235], v[220:223], v[56:59]
	v_pk_max_i16 v42, v42, 0
	v_pk_max_i16 v43, v43, 0
	s_waitcnt lgkmcnt(4)
	v_mfma_f32_16x16x32_bf16 v[68:71], v[236:239], v[216:219], v[68:71]
	v_pk_max_i16 v44, v44, 0
	v_pk_max_i16 v45, v45, 0
	v_mfma_f32_16x16x32_bf16 v[60:63], v[236:239], v[220:223], v[60:63]
	v_pk_max_i16 v46, v46, 0
	v_pk_max_i16 v47, v47, 0
	s_cmp_lt_u32 s31, 2
	s_cbranch_scc0 .Lnerf_hid_b_first
	s_waitcnt vmcnt(0) lgkmcnt(0)
	s_barrier
	ds_read_b128 v[224:227], v121 offset:40960
	ds_read_b128 v[228:231], v121 offset:41984
	ds_read_b128 v[152:155], v183 offset:0
	ds_read_b128 v[156:159], v183 offset:64
	v_mfma_f32_16x16x32_bf16 v[80:83], v[240:243], v[208:211], 0
	ds_read_b128 v[232:235], v121 offset:43008
	v_cvt_pk_bf16_f32 v48, v64, v65
	v_cvt_pk_bf16_f32 v49, v66, v67
	v_mfma_f32_16x16x32_bf16 v[84:87], v[240:243], v[212:215], 0
	ds_read_b128 v[236:239], v121 offset:44032
	v_cvt_pk_bf16_f32 v52, v56, v57
	v_cvt_pk_bf16_f32 v53, v58, v59
	ds_read_b128 v[240:243], v121 offset:45056
	v_mfma_f32_16x16x32_bf16 v[76:79], v[244:247], v[208:211], 0
	v_cvt_pk_bf16_f32 v50, v68, v69
	v_cvt_pk_bf16_f32 v51, v70, v71
	v_mfma_f32_16x16x32_bf16 v[72:75], v[244:247], v[212:215], 0
	v_cvt_pk_bf16_f32 v54, v60, v61
	v_cvt_pk_bf16_f32 v55, v62, v63
	ds_read_b128 v[244:247], v121 offset:46080
	v_mfma_f32_16x16x32_bf16 v[80:83], v[248:251], v[216:219], v[80:83]
	v_pk_max_i16 v48, v48, 0
	v_pk_max_i16 v49, v49, 0
	v_mfma_f32_16x16x32_bf16 v[84:87], v[248:251], v[220:223], v[84:87]
	v_pk_max_i16 v50, v50, 0
	v_pk_max_i16 v51, v51, 0
	ds_read_b128 v[248:251], v121 offset:47104
	v_mfma_f32_16x16x32_bf16 v[76:79], v[252:255], v[216:219], v[76:79]
	v_pk_max_i16 v52, v52, 0
	v_pk_max_i16 v53, v53, 0
	v_mfma_f32_16x16x32_bf16 v[72:75], v[252:255], v[220:223], v[72:75]
	v_pk_max_i16 v54, v54, 0
	v_pk_max_i16 v55, v55, 0
	ds_read_b128 v[252:255], v121 offset:48128
	s_setprio 3
	s_waitcnt lgkmcnt(6)
	v_mfma_f32_16x16x32_bf16 v[64:67], v[224:227], v[0:3], v[152:155]
	v_mfma_f32_16x16x32_bf16 v[68:71], v[228:231], v[0:3], v[156:159]
	v_mfma_f32_16x16x32_bf16 v[60:63], v[228:231], v[4:7], v[156:159]
	v_mfma_f32_16x16x32_bf16 v[56:59], v[224:227], v[4:7], v[152:155]
	ds_read_b128 v[224:227], v121 offset:49152
	ds_read_b128 v[228:231], v121 offset:50176
	s_waitcnt lgkmcnt(6)
	ds_read_b128 v[160:163], v183 offset:128
	ds_read_b128 v[164:167], v183 offset:192
	v_mfma_f32_16x16x32_bf16 v[64:67], v[232:235], v[12:15], v[64:67]
	v_cvt_pk_bf16_f32 v112, v80, v81
	v_mfma_f32_16x16x32_bf16 v[68:71], v[236:239], v[12:15], v[68:71]
	s_mov_b32 m0, s35
	s_add_i32 s51, s50, 0x0
	v_cvt_pk_bf16_f32 v113, v82, v83
	v_mfma_f32_16x16x32_bf16 v[60:63], v[236:239], v[8:11], v[60:63]
	buffer_load_dwordx4 v125, s[36:39], s51 offen lds
	v_cvt_pk_bf16_f32 v114, v76, v77
	v_mfma_f32_16x16x32_bf16 v[56:59], v[232:235], v[8:11], v[56:59]
	v_cvt_pk_bf16_f32 v115, v78, v79
	ds_read_b128 v[232:235], v121 offset:51200
	ds_read_b128 v[236:239], v121 offset:52224
	s_waitcnt lgkmcnt(8)
	v_mfma_f32_16x16x32_bf16 v[64:67], v[240:243], v[16:19], v[64:67]
	v_cvt_pk_bf16_f32 v116, v84, v85
	v_mfma_f32_16x16x32_bf16 v[68:71], v[244:247], v[16:19], v[68:71]
	s_mov_b32 m0, s42
	s_add_i32 s51, s50, 0x2000
	v_cvt_pk_bf16_f32 v117, v86, v87
	v_mfma_f32_16x16x32_bf16 v[60:63], v[244:247], v[20:23], v[60:63]
	buffer_load_dwordx4 v125, s[36:39], s51 offen lds
	v_cvt_pk_bf16_f32 v118, v72, v73
	v_mfma_f32_16x16x32_bf16 v[56:59], v[240:243], v[20:23], v[56:59]
	v_cvt_pk_bf16_f32 v119, v74, v75
	ds_read_b128 v[240:243], v121 offset:53248
	ds_read_b128 v[244:247], v121 offset:54272
	s_waitcnt lgkmcnt(8)
	v_mfma_f32_16x16x32_bf16 v[64:67], v[248:251], v[24:27], v[64:67]
	v_pk_max_i16 v112, v112, 0
	v_mfma_f32_16x16x32_bf16 v[68:71], v[252:255], v[24:27], v[68:71]
	s_mov_b32 m0, s41
	s_add_i32 s51, s50, 0x4000
	v_pk_max_i16 v113, v113, 0
	v_mfma_f32_16x16x32_bf16 v[60:63], v[252:255], v[28:31], v[60:63]
	buffer_load_dwordx4 v125, s[36:39], s51 offen lds
	v_pk_max_i16 v114, v114, 0
	v_mfma_f32_16x16x32_bf16 v[56:59], v[248:251], v[28:31], v[56:59]
	v_pk_max_i16 v115, v115, 0
	ds_read_b128 v[248:251], v121 offset:55296
	ds_read_b128 v[252:255], v121 offset:56320
	s_setprio 2
	s_waitcnt lgkmcnt(8)
	v_mfma_f32_16x16x32_bf16 v[64:67], v[224:227], v[32:35], v[64:67]
	v_pk_max_i16 v116, v116, 0
	v_mfma_f32_16x16x32_bf16 v[68:71], v[228:231], v[32:35], v[68:71]
	s_mov_b32 m0, s40
	s_add_i32 s51, s50, 0x6000
	v_pk_max_i16 v117, v117, 0
	v_mfma_f32_16x16x32_bf16 v[60:63], v[228:231], v[36:39], v[60:63]
	buffer_load_dwordx4 v125, s[36:39], s51 offen lds
	v_pk_max_i16 v118, v118, 0
	v_mfma_f32_16x16x32_bf16 v[56:59], v[224:227], v[36:39], v[56:59]
	v_pk_max_i16 v119, v119, 0
	ds_read_b128 v[224:227], v121 offset:57344
	ds_read_b128 v[228:231], v121 offset:58368
	s_waitcnt lgkmcnt(6)
	v_mfma_f32_16x16x32_bf16 v[64:67], v[232:235], v[40:43], v[64:67]
	v_mfma_f32_16x16x32_bf16 v[68:71], v[236:239], v[40:43], v[68:71]
	v_mfma_f32_16x16x32_bf16 v[60:63], v[236:239], v[44:47], v[60:63]
	v_mfma_f32_16x16x32_bf16 v[56:59], v[232:235], v[44:47], v[56:59]
	ds_read_b128 v[232:235], v121 offset:59392
	ds_read_b128 v[236:239], v121 offset:60416
	s_waitcnt lgkmcnt(6)
	ds_read_b128 v[152:155], v183 offset:256
	ds_read_b128 v[156:159], v183 offset:320
	v_mfma_f32_16x16x32_bf16 v[64:67], v[240:243], v[48:51], v[64:67]
	v_mfma_f32_16x16x32_bf16 v[68:71], v[244:247], v[48:51], v[68:71]
	v_mfma_f32_16x16x32_bf16 v[60:63], v[244:247], v[52:55], v[60:63]
	v_mfma_f32_16x16x32_bf16 v[56:59], v[240:243], v[52:55], v[56:59]
	ds_read_b128 v[240:243], v121 offset:61440
	ds_read_b128 v[244:247], v121 offset:62464
	s_waitcnt lgkmcnt(8)
	v_mfma_f32_16x16x32_bf16 v[64:67], v[248:251], v[112:115], v[64:67]
	v_mfma_f32_16x16x32_bf16 v[68:71], v[252:255], v[112:115], v[68:71]
	v_mfma_f32_16x16x32_bf16 v[60:63], v[252:255], v[116:119], v[60:63]
	v_mfma_f32_16x16x32_bf16 v[56:59], v[248:251], v[116:119], v[56:59]
	ds_read_b128 v[248:251], v121 offset:63488
	ds_read_b128 v[252:255], v121 offset:64512
	s_setprio 1
	s_waitcnt lgkmcnt(8)
	v_mfma_f32_16x16x32_bf16 v[80:83], v[224:227], v[0:3], v[160:163]
	v_mfma_f32_16x16x32_bf16 v[76:79], v[228:231], v[0:3], v[164:167]
	v_mfma_f32_16x16x32_bf16 v[72:75], v[228:231], v[4:7], v[164:167]
	v_mfma_f32_16x16x32_bf16 v[84:87], v[224:227], v[4:7], v[160:163]
	ds_read_b128 v[224:227], v126 offset:57344
	ds_read_b128 v[228:231], v126 offset:58368
	s_waitcnt lgkmcnt(8)
	v_mfma_f32_16x16x32_bf16 v[80:83], v[232:235], v[12:15], v[80:83]
	v_cvt_pk_bf16_f32 v88, v64, v65
	v_mfma_f32_16x16x32_bf16 v[76:79], v[236:239], v[12:15], v[76:79]
	v_cvt_pk_bf16_f32 v89, v66, v67
	v_mfma_f32_16x16x32_bf16 v[72:75], v[236:239], v[8:11], v[72:75]
	v_cvt_pk_bf16_f32 v90, v68, v69
	v_mfma_f32_16x16x32_bf16 v[84:87], v[232:235], v[8:11], v[84:87]
	v_cvt_pk_bf16_f32 v91, v70, v71
	ds_read_b128 v[232:235], v126 offset:59392
	ds_read_b128 v[236:239], v126 offset:60416
	s_waitcnt lgkmcnt(6)
	v_mfma_f32_16x16x32_bf16 v[80:83], v[240:243], v[16:19], v[80:83]
	v_cvt_pk_bf16_f32 v92, v56, v57
	v_mfma_f32_16x16x32_bf16 v[76:79], v[244:247], v[16:19], v[76:79]
	v_cvt_pk_bf16_f32 v93, v58, v59
	v_mfma_f32_16x16x32_bf16 v[72:75], v[244:247], v[20:23], v[72:75]
	v_cvt_pk_bf16_f32 v94, v60, v61
	v_mfma_f32_16x16x32_bf16 v[84:87], v[240:243], v[20:23], v[84:87]
	v_cvt_pk_bf16_f32 v95, v62, v63
	ds_read_b128 v[240:243], v126 offset:61440
	ds_read_b128 v[244:247], v126 offset:62464
	s_waitcnt lgkmcnt(6)
	v_mfma_f32_16x16x32_bf16 v[80:83], v[248:251], v[24:27], v[80:83]
	v_pk_max_i16 v88, v88, 0
	v_mfma_f32_16x16x32_bf16 v[76:79], v[252:255], v[24:27], v[76:79]
	v_pk_max_i16 v89, v89, 0
	v_mfma_f32_16x16x32_bf16 v[72:75], v[252:255], v[28:31], v[72:75]
	v_pk_max_i16 v90, v90, 0
	v_mfma_f32_16x16x32_bf16 v[84:87], v[248:251], v[28:31], v[84:87]
	v_pk_max_i16 v91, v91, 0
	ds_read_b128 v[248:251], v126 offset:63488
	ds_read_b128 v[252:255], v126 offset:64512
	s_setprio 0
	s_waitcnt lgkmcnt(6)
	v_mfma_f32_16x16x32_bf16 v[80:83], v[224:227], v[32:35], v[80:83]
	v_pk_max_i16 v92, v92, 0
	v_mfma_f32_16x16x32_bf16 v[76:79], v[228:231], v[32:35], v[76:79]
	v_pk_max_i16 v93, v93, 0
	v_mfma_f32_16x16x32_bf16 v[72:75], v[228:231], v[36:39], v[72:75]
	v_pk_max_i16 v94, v94, 0
	v_mfma_f32_16x16x32_bf16 v[84:87], v[224:227], v[36:39], v[84:87]
	v_pk_max_i16 v95, v95, 0
	s_waitcnt lgkmcnt(4)
	v_mfma_f32_16x16x32_bf16 v[80:83], v[232:235], v[40:43], v[80:83]
	v_mfma_f32_16x16x32_bf16 v[76:79], v[236:239], v[40:43], v[76:79]
	v_mfma_f32_16x16x32_bf16 v[72:75], v[236:239], v[44:47], v[72:75]
	v_mfma_f32_16x16x32_bf16 v[84:87], v[232:235], v[44:47], v[84:87]
	s_branch .Lnerf_hid_a1

.Lnerf_hid_a3:
	s_waitcnt vmcnt(0) lgkmcnt(0)
	s_barrier
	ds_read_b128 v[224:227], v121 offset:8192
	ds_read_b128 v[228:231], v121 offset:9216
	v_mfma_f32_16x16x32_bf16 v[80:83], v[240:243], v[48:51], v[80:83]
	ds_read_b128 v[232:235], v121 offset:10240
	v_mfma_f32_16x16x32_bf16 v[76:79], v[244:247], v[48:51], v[76:79]
	ds_read_b128 v[236:239], v121 offset:11264
	v_mfma_f32_16x16x32_bf16 v[72:75], v[244:247], v[52:55], v[72:75]
	v_mfma_f32_16x16x32_bf16 v[84:87], v[240:243], v[52:55], v[84:87]
	ds_read_b128 v[240:243], v121 offset:12288
	ds_read_b128 v[244:247], v121 offset:13312
	v_mfma_f32_16x16x32_bf16 v[80:83], v[248:251], v[112:115], v[80:83]
	v_mfma_f32_16x16x32_bf16 v[76:79], v[252:255], v[112:115], v[76:79]
	v_mfma_f32_16x16x32_bf16 v[72:75], v[252:255], v[116:119], v[72:75]
	v_mfma_f32_16x16x32_bf16 v[84:87], v[248:251], v[116:119], v[84:87]
	ds_read_b128 v[248:251], v121 offset:14336
	ds_read_b128 v[252:255], v121 offset:15360
	s_setprio 3
	s_waitcnt lgkmcnt(6)
	v_mfma_f32_16x16x32_bf16 v[64:67], v[224:227], v[0:3], v[152:155]
	v_mfma_f32_16x16x32_bf16 v[68:71], v[228:231], v[0:3], v[156:159]
	v_mfma_f32_16x16x32_bf16 v[60:63], v[228:231], v[4:7], v[156:159]
	v_mfma_f32_16x16x32_bf16 v[56:59], v[224:227], v[4:7], v[152:155]
	ds_read_b128 v[224:227], v121 offset:16384
	ds_read_b128 v[228:231], v121 offset:17408
	s_waitcnt lgkmcnt(6)
	ds_read_b128 v[160:163], v183 offset:896
	ds_read_b128 v[164:167], v183 offset:960
	v_mfma_f32_16x16x32_bf16 v[64:67], v[232:235], v[12:15], v[64:67]
	v_mfma_f32_16x16x32_bf16 v[68:71], v[236:239], v[12:15], v[68:71]
	s_mov_b32 m0, s28
	s_add_i32 s51, s50, 0x18000
	s_cmp_eq_u32 s52, 3
	s_cselect_b32 s51, 0x8000, s51
	v_mfma_f32_16x16x32_bf16 v[60:63], v[236:239], v[8:11], v[60:63]
	buffer_load_dwordx4 v125, s[36:39], s51 offen lds
	v_mfma_f32_16x16x32_bf16 v[56:59], v[232:235], v[8:11], v[56:59]
	ds_read_b128 v[232:235], v121 offset:18432
	ds_read_b128 v[236:239], v121 offset:19456
	s_waitcnt lgkmcnt(8)
	v_mfma_f32_16x16x32_bf16 v[64:67], v[240:243], v[16:19], v[64:67]
	v_mfma_f32_16x16x32_bf16 v[68:71], v[244:247], v[16:19], v[68:71]
	s_mov_b32 m0, s29
	s_add_i32 s51, s50, 0x1a000
	s_cmp_eq_u32 s52, 3
	s_cselect_b32 s51, 0xa000, s51
	v_mfma_f32_16x16x32_bf16 v[60:63], v[244:247], v[20:23], v[60:63]
	buffer_load_dwordx4 v125, s[36:39], s51 offen lds
	v_mfma_f32_16x16x32_bf16 v[56:59], v[240:243], v[20:23], v[56:59]
	ds_read_b128 v[240:243], v121 offset:20480
	ds_read_b128 v[244:247], v121 offset:21504
	s_waitcnt lgkmcnt(8)
	v_mfma_f32_16x16x32_bf16 v[64:67], v[248:251], v[24:27], v[64:67]
	v_mfma_f32_16x16x32_bf16 v[68:71], v[252:255], v[24:27], v[68:71]
	s_mov_b32 m0, s33
	s_add_i32 s51, s50, 0x1c000
	s_cmp_eq_u32 s52, 3
	s_cselect_b32 s51, 0xc000, s51
	v_mfma_f32_16x16x32_bf16 v[60:63], v[252:255], v[28:31], v[60:63]
	buffer_load_dwordx4 v125, s[36:39], s51 offen lds
	v_mfma_f32_16x16x32_bf16 v[56:59], v[248:251], v[28:31], v[56:59]
	ds_read_b128 v[248:251], v121 offset:22528
	ds_read_b128 v[252:255], v121 offset:23552
	s_setprio 2
	s_waitcnt lgkmcnt(8)
	v_mfma_f32_16x16x32_bf16 v[64:67], v[224:227], v[32:35], v[64:67]
	v_mfma_f32_16x16x32_bf16 v[68:71], v[228:231], v[32:35], v[68:71]
	s_mov_b32 m0, s34
	s_add_i32 s51, s50, 0x1e000
	s_cmp_eq_u32 s52, 3
	s_cselect_b32 s51, 0xe000, s51
	v_mfma_f32_16x16x32_bf16 v[60:63], v[228:231], v[36:39], v[60:63]
	buffer_load_dwordx4 v125, s[36:39], s51 offen lds
	v_mfma_f32_16x16x32_bf16 v[56:59], v[224:227], v[36:39], v[56:59]
	ds_read_b128 v[224:227], v121 offset:24576
	ds_read_b128 v[228:231], v121 offset:25600
	s_waitcnt lgkmcnt(6)
	v_mfma_f32_16x16x32_bf16 v[64:67], v[232:235], v[40:43], v[64:67]
	v_cvt_pk_bf16_f32 v200, v80, v81
	v_mfma_f32_16x16x32_bf16 v[68:71], v[236:239], v[40:43], v[68:71]
	v_cvt_pk_bf16_f32 v201, v82, v83
	v_mfma_f32_16x16x32_bf16 v[60:63], v[236:239], v[44:47], v[60:63]
	v_cvt_pk_bf16_f32 v202, v76, v77
	v_mfma_f32_16x16x32_bf16 v[56:59], v[232:235], v[44:47], v[56:59]
	v_cvt_pk_bf16_f32 v203, v78, v79
	ds_read_b128 v[232:235], v121 offset:26624
	ds_read_b128 v[236:239], v121 offset:27648
	s_waitcnt lgkmcnt(6)
	ds_read_b128 v[152:155], v183 offset:1024
	ds_read_b128 v[156:159], v183 offset:1088
	v_mfma_f32_16x16x32_bf16 v[64:67], v[240:243], v[48:51], v[64:67]
	v_cvt_pk_bf16_f32 v204, v84, v85
	v_mfma_f32_16x16x32_bf16 v[68:71], v[244:247], v[48:51], v[68:71]
	v_cvt_pk_bf16_f32 v205, v86, v87
	v_mfma_f32_16x16x32_bf16 v[60:63], v[244:247], v[52:55], v[60:63]
	v_cvt_pk_bf16_f32 v206, v72, v73
	v_mfma_f32_16x16x32_bf16 v[56:59], v[240:243], v[52:55], v[56:59]
	v_cvt_pk_bf16_f32 v207, v74, v75
	ds_read_b128 v[240:243], v121 offset:28672
	ds_read_b128 v[244:247], v121 offset:29696
	s_waitcnt lgkmcnt(8)
	v_mfma_f32_16x16x32_bf16 v[64:67], v[248:251], v[112:115], v[64:67]
	v_pk_max_i16 v200, v200, 0
	v_mfma_f32_16x16x32_bf16 v[68:71], v[252:255], v[112:115], v[68:71]
	v_pk_max_i16 v201, v201, 0
	v_mfma_f32_16x16x32_bf16 v[60:63], v[252:255], v[116:119], v[60:63]
	v_pk_max_i16 v202, v202, 0
	v_mfma_f32_16x16x32_bf16 v[56:59], v[248:251], v[116:119], v[56:59]
	v_pk_max_i16 v203, v203, 0
	ds_read_b128 v[248:251], v121 offset:30720
	ds_read_b128 v[252:255], v121 offset:31744
	s_setprio 1
	s_waitcnt lgkmcnt(8)
	v_mfma_f32_16x16x32_bf16 v[80:83], v[224:227], v[0:3], v[160:163]
	v_pk_max_i16 v204, v204, 0
	v_mfma_f32_16x16x32_bf16 v[76:79], v[228:231], v[0:3], v[164:167]
	v_pk_max_i16 v205, v205, 0
	v_mfma_f32_16x16x32_bf16 v[72:75], v[228:231], v[4:7], v[164:167]
	v_pk_max_i16 v206, v206, 0
	v_mfma_f32_16x16x32_bf16 v[84:87], v[224:227], v[4:7], v[160:163]
	v_pk_max_i16 v207, v207, 0
	ds_read_b128 v[224:227], v121 offset:32768
	ds_read_b128 v[228:231], v121 offset:33792
	s_waitcnt lgkmcnt(8)
	v_mfma_f32_16x16x32_bf16 v[80:83], v[232:235], v[12:15], v[80:83]
	v_cvt_pk_bf16_f32 v208, v64, v65
	v_mfma_f32_16x16x32_bf16 v[76:79], v[236:239], v[12:15], v[76:79]
	v_cvt_pk_bf16_f32 v209, v66, v67
	v_mfma_f32_16x16x32_bf16 v[72:75], v[236:239], v[8:11], v[72:75]
	v_cvt_pk_bf16_f32 v210, v68, v69
	v_mfma_f32_16x16x32_bf16 v[84:87], v[232:235], v[8:11], v[84:87]
	v_cvt_pk_bf16_f32 v211, v70, v71
	ds_read_b128 v[232:235], v121 offset:34816
	ds_read_b128 v[236:239], v121 offset:35840
	s_waitcnt lgkmcnt(6)
	v_mfma_f32_16x16x32_bf16 v[80:83], v[240:243], v[16:19], v[80:83]
	v_cvt_pk_bf16_f32 v212, v56, v57
	v_mfma_f32_16x16x32_bf16 v[76:79], v[244:247], v[16:19], v[76:79]
	v_cvt_pk_bf16_f32 v213, v58, v59
	v_mfma_f32_16x16x32_bf16 v[72:75], v[244:247], v[20:23], v[72:75]
	v_cvt_pk_bf16_f32 v214, v60, v61
	v_mfma_f32_16x16x32_bf16 v[84:87], v[240:243], v[20:23], v[84:87]
	v_cvt_pk_bf16_f32 v215, v62, v63
	ds_read_b128 v[240:243], v121 offset:36864
	ds_read_b128 v[244:247], v121 offset:37888
	s_waitcnt lgkmcnt(6)
	v_mfma_f32_16x16x32_bf16 v[80:83], v[248:251], v[24:27], v[80:83]
	v_pk_max_i16 v208, v208, 0
	v_mfma_f32_16x16x32_bf16 v[76:79], v[252:255], v[24:27], v[76:79]
	v_pk_max_i16 v209, v209, 0
	v_mfma_f32_16x16x32_bf16 v[72:75], v[252:255], v[28:31], v[72:75]
	v_pk_max_i16 v210, v210, 0
	v_mfma_f32_16x16x32_bf16 v[84:87], v[248:251], v[28:31], v[84:87]
	v_pk_max_i16 v211, v211, 0
	ds_read_b128 v[248:251], v121 offset:38912
	ds_read_b128 v[252:255], v121 offset:39936
	s_setprio 0
	s_waitcnt lgkmcnt(6)
	v_mfma_f32_16x16x32_bf16 v[80:83], v[224:227], v[32:35], v[80:83]
	v_pk_max_i16 v212, v212, 0
	v_mfma_f32_16x16x32_bf16 v[76:79], v[228:231], v[32:35], v[76:79]
	v_pk_max_i16 v213, v213, 0
	v_mfma_f32_16x16x32_bf16 v[72:75], v[228:231], v[36:39], v[72:75]
	v_pk_max_i16 v214, v214, 0
	v_mfma_f32_16x16x32_bf16 v[84:87], v[224:227], v[36:39], v[84:87]
	v_pk_max_i16 v215, v215, 0
	s_waitcnt lgkmcnt(4)
	v_mfma_f32_16x16x32_bf16 v[80:83], v[232:235], v[40:43], v[80:83]
	v_mfma_f32_16x16x32_bf16 v[76:79], v[236:239], v[40:43], v[76:79]
	v_mfma_f32_16x16x32_bf16 v[72:75], v[236:239], v[44:47], v[72:75]
	v_mfma_f32_16x16x32_bf16 v[84:87], v[232:235], v[44:47], v[84:87]
	s_cmp_eq_u32 s52, 3
	s_cbranch_scc1 .Lnerf_head

.Lnerf_hid_b3:
	s_waitcnt vmcnt(0) lgkmcnt(0)
	s_barrier
	ds_read_b128 v[224:227], v121 offset:8192
	ds_read_b128 v[228:231], v121 offset:9216
	v_mfma_f32_16x16x32_bf16 v[80:83], v[240:243], v[48:51], v[80:83]
	ds_read_b128 v[232:235], v121 offset:10240
	v_mfma_f32_16x16x32_bf16 v[76:79], v[244:247], v[48:51], v[76:79]
	ds_read_b128 v[236:239], v121 offset:11264
	v_mfma_f32_16x16x32_bf16 v[72:75], v[244:247], v[52:55], v[72:75]
	v_mfma_f32_16x16x32_bf16 v[84:87], v[240:243], v[52:55], v[84:87]
	ds_read_b128 v[240:243], v121 offset:12288
	ds_read_b128 v[244:247], v121 offset:13312
	v_mfma_f32_16x16x32_bf16 v[80:83], v[248:251], v[112:115], v[80:83]
	v_mfma_f32_16x16x32_bf16 v[76:79], v[252:255], v[112:115], v[76:79]
	v_mfma_f32_16x16x32_bf16 v[72:75], v[252:255], v[116:119], v[72:75]
	v_mfma_f32_16x16x32_bf16 v[84:87], v[248:251], v[116:119], v[84:87]
	ds_read_b128 v[248:251], v121 offset:14336
	ds_read_b128 v[252:255], v121 offset:15360
	s_setprio 3
	s_waitcnt lgkmcnt(6)
	v_mfma_f32_16x16x32_bf16 v[64:67], v[224:227], v[0:3], v[152:155]
	v_mfma_f32_16x16x32_bf16 v[68:71], v[228:231], v[0:3], v[156:159]
	v_mfma_f32_16x16x32_bf16 v[60:63], v[228:231], v[4:7], v[156:159]
	v_mfma_f32_16x16x32_bf16 v[56:59], v[224:227], v[4:7], v[152:155]
	ds_read_b128 v[224:227], v121 offset:16384
	ds_read_b128 v[228:231], v121 offset:17408
	s_waitcnt lgkmcnt(6)
	ds_read_b128 v[160:163], v183 offset:896
	ds_read_b128 v[164:167], v183 offset:960
	v_mfma_f32_16x16x32_bf16 v[64:67], v[232:235], v[12:15], v[64:67]
	v_cvt_pk_bf16_f32 v200, v80, v81
	v_mfma_f32_16x16x32_bf16 v[68:71], v[236:239], v[12:15], v[68:71]
	v_cvt_pk_bf16_f32 v201, v82, v83
	v_mfma_f32_16x16x32_bf16 v[60:63], v[236:239], v[8:11], v[60:63]
	v_cvt_pk_bf16_f32 v202, v76, v77
	v_mfma_f32_16x16x32_bf16 v[56:59], v[232:235], v[8:11], v[56:59]
	v_cvt_pk_bf16_f32 v203, v78, v79
	ds_read_b128 v[232:235], v121 offset:18432
	ds_read_b128 v[236:239], v121 offset:19456
	s_waitcnt lgkmcnt(8)
	v_mfma_f32_16x16x32_bf16 v[64:67], v[240:243], v[16:19], v[64:67]
	v_cvt_pk_bf16_f32 v204, v84, v85
	v_mfma_f32_16x16x32_bf16 v[68:71], v[244:247], v[16:19], v[68:71]
	v_cvt_pk_bf16_f32 v205, v86, v87
	v_mfma_f32_16x16x32_bf16 v[60:63], v[244:247], v[20:23], v[60:63]
	v_cvt_pk_bf16_f32 v206, v72, v73
	v_mfma_f32_16x16x32_bf16 v[56:59], v[240:243], v[20:23], v[56:59]
	v_cvt_pk_bf16_f32 v207, v74, v75
	ds_read_b128 v[240:243], v121 offset:20480
	ds_read_b128 v[244:247], v121 offset:21504
	s_waitcnt lgkmcnt(8)
	v_mfma_f32_16x16x32_bf16 v[64:67], v[248:251], v[24:27], v[64:67]
	v_pk_max_i16 v200, v200, 0
	v_mfma_f32_16x16x32_bf16 v[68:71], v[252:255], v[24:27], v[68:71]
	v_pk_max_i16 v201, v201, 0
	v_mfma_f32_16x16x32_bf16 v[60:63], v[252:255], v[28:31], v[60:63]
	v_pk_max_i16 v202, v202, 0
	v_mfma_f32_16x16x32_bf16 v[56:59], v[248:251], v[28:31], v[56:59]
	v_pk_max_i16 v203, v203, 0
	ds_read_b128 v[248:251], v121 offset:22528
	ds_read_b128 v[252:255], v121 offset:23552
	s_setprio 2
	s_waitcnt lgkmcnt(8)
	v_mfma_f32_16x16x32_bf16 v[64:67], v[224:227], v[32:35], v[64:67]
	v_pk_max_i16 v204, v204, 0
	v_mfma_f32_16x16x32_bf16 v[68:71], v[228:231], v[32:35], v[68:71]
	v_pk_max_i16 v205, v205, 0
	v_mfma_f32_16x16x32_bf16 v[60:63], v[228:231], v[36:39], v[60:63]
	v_pk_max_i16 v206, v206, 0
	v_mfma_f32_16x16x32_bf16 v[56:59], v[224:227], v[36:39], v[56:59]
	v_pk_max_i16 v207, v207, 0
	ds_read_b128 v[224:227], v121 offset:24576
	ds_read_b128 v[228:231], v121 offset:25600
	s_waitcnt lgkmcnt(6)
	v_mfma_f32_16x16x32_bf16 v[64:67], v[232:235], v[40:43], v[64:67]
	v_mfma_f32_16x16x32_bf16 v[68:71], v[236:239], v[40:43], v[68:71]
	s_mov_b32 m0, s28
	s_add_i32 s51, s50, 0x18000
	s_cmp_eq_u32 s52, 3
	s_cselect_b32 s51, 0x8000, s51
	v_mfma_f32_16x16x32_bf16 v[60:63], v[236:239], v[44:47], v[60:63]
	buffer_load_dwordx4 v125, s[36:39], s51 offen lds
	v_mfma_f32_16x16x32_bf16 v[56:59], v[232:235], v[44:47], v[56:59]
	ds_read_b128 v[232:235], v121 offset:26624
	ds_read_b128 v[236:239], v121 offset:27648
	s_waitcnt lgkmcnt(6)
	ds_read_b128 v[152:155], v183 offset:1024
	ds_read_b128 v[156:159], v183 offset:1088
	v_mfma_f32_16x16x32_bf16 v[64:67], v[240:243], v[48:51], v[64:67]
	v_mfma_f32_16x16x32_bf16 v[68:71], v[244:247], v[48:51], v[68:71]
	s_mov_b32 m0, s29
	s_add_i32 s51, s50, 0x1a000
	s_cmp_eq_u32 s52, 3
	s_cselect_b32 s51, 0xa000, s51
	v_mfma_f32_16x16x32_bf16 v[60:63], v[244:247], v[52:55], v[60:63]
	buffer_load_dwordx4 v125, s[36:39], s51 offen lds
	v_mfma_f32_16x16x32_bf16 v[56:59], v[240:243], v[52:55], v[56:59]
	ds_read_b128 v[240:243], v121 offset:28672
	ds_read_b128 v[244:247], v121 offset:29696
	s_waitcnt lgkmcnt(8)
	v_mfma_f32_16x16x32_bf16 v[64:67], v[248:251], v[112:115], v[64:67]
	v_mfma_f32_16x16x32_bf16 v[68:71], v[252:255], v[112:115], v[68:71]
	s_mov_b32 m0, s33
	s_add_i32 s51, s50, 0x1c000
	s_cmp_eq_u32 s52, 3
	s_cselect_b32 s51, 0xc000, s51
	v_mfma_f32_16x16x32_bf16 v[60:63], v[252:255], v[116:119], v[60:63]
	buffer_load_dwordx4 v125, s[36:39], s51 offen lds
	v_mfma_f32_16x16x32_bf16 v[56:59], v[248:251], v[116:119], v[56:59]
	ds_read_b128 v[248:251], v121 offset:30720
	ds_read_b128 v[252:255], v121 offset:31744
	s_setprio 1
	s_waitcnt lgkmcnt(8)
	v_mfma_f32_16x16x32_bf16 v[80:83], v[224:227], v[0:3], v[160:163]
	v_mfma_f32_16x16x32_bf16 v[76:79], v[228:231], v[0:3], v[164:167]
	s_mov_b32 m0, s34
	s_add_i32 s51, s50, 0x1e000
	s_cmp_eq_u32 s52, 3
	s_cselect_b32 s51, 0xe000, s51
	v_mfma_f32_16x16x32_bf16 v[72:75], v[228:231], v[4:7], v[164:167]
	buffer_load_dwordx4 v125, s[36:39], s51 offen lds
	v_mfma_f32_16x16x32_bf16 v[84:87], v[224:227], v[4:7], v[160:163]
	ds_read_b128 v[224:227], v121 offset:32768
	ds_read_b128 v[228:231], v121 offset:33792
	s_waitcnt lgkmcnt(8)
	v_mfma_f32_16x16x32_bf16 v[80:83], v[232:235], v[12:15], v[80:83]
	v_cvt_pk_bf16_f32 v208, v64, v65
	v_mfma_f32_16x16x32_bf16 v[76:79], v[236:239], v[12:15], v[76:79]
	v_cvt_pk_bf16_f32 v209, v66, v67
	v_mfma_f32_16x16x32_bf16 v[72:75], v[236:239], v[8:11], v[72:75]
	v_cvt_pk_bf16_f32 v210, v68, v69
	v_mfma_f32_16x16x32_bf16 v[84:87], v[232:235], v[8:11], v[84:87]
	v_cvt_pk_bf16_f32 v211, v70, v71
	ds_read_b128 v[232:235], v121 offset:34816
	ds_read_b128 v[236:239], v121 offset:35840
	s_waitcnt lgkmcnt(6)
	v_mfma_f32_16x16x32_bf16 v[80:83], v[240:243], v[16:19], v[80:83]
	v_cvt_pk_bf16_f32 v212, v56, v57
	v_mfma_f32_16x16x32_bf16 v[76:79], v[244:247], v[16:19], v[76:79]
	v_cvt_pk_bf16_f32 v213, v58, v59
	v_mfma_f32_16x16x32_bf16 v[72:75], v[244:247], v[20:23], v[72:75]
	v_cvt_pk_bf16_f32 v214, v60, v61
	v_mfma_f32_16x16x32_bf16 v[84:87], v[240:243], v[20:23], v[84:87]
	v_cvt_pk_bf16_f32 v215, v62, v63
	ds_read_b128 v[240:243], v121 offset:36864
	ds_read_b128 v[244:247], v121 offset:37888
	s_waitcnt lgkmcnt(6)
	v_mfma_f32_16x16x32_bf16 v[80:83], v[248:251], v[24:27], v[80:83]
	v_pk_max_i16 v208, v208, 0
	v_mfma_f32_16x16x32_bf16 v[76:79], v[252:255], v[24:27], v[76:79]
	v_pk_max_i16 v209, v209, 0
	v_mfma_f32_16x16x32_bf16 v[72:75], v[252:255], v[28:31], v[72:75]
	v_pk_max_i16 v210, v210, 0
	v_mfma_f32_16x16x32_bf16 v[84:87], v[248:251], v[28:31], v[84:87]
	v_pk_max_i16 v211, v211, 0
	ds_read_b128 v[248:251], v121 offset:38912
	ds_read_b128 v[252:255], v121 offset:39936
	s_setprio 0
	s_waitcnt lgkmcnt(6)
	v_mfma_f32_16x16x32_bf16 v[80:83], v[224:227], v[32:35], v[80:83]
	v_pk_max_i16 v212, v212, 0
	v_mfma_f32_16x16x32_bf16 v[76:79], v[228:231], v[32:35], v[76:79]
	v_pk_max_i16 v213, v213, 0
	v_mfma_f32_16x16x32_bf16 v[72:75], v[228:231], v[36:39], v[72:75]
	v_pk_max_i16 v214, v214, 0
	v_mfma_f32_16x16x32_bf16 v[84:87], v[224:227], v[36:39], v[84:87]
	v_pk_max_i16 v215, v215, 0
	s_waitcnt lgkmcnt(4)
	v_mfma_f32_16x16x32_bf16 v[80:83], v[232:235], v[40:43], v[80:83]
	v_mfma_f32_16x16x32_bf16 v[76:79], v[236:239], v[40:43], v[76:79]
	v_mfma_f32_16x16x32_bf16 v[72:75], v[236:239], v[44:47], v[72:75]
	v_mfma_f32_16x16x32_bf16 v[84:87], v[232:235], v[44:47], v[84:87]
	s_cmp_eq_u32 s52, 3
	s_cbranch_scc1 .Lnerf_head
